# agg1: 40 index slots preloaded (no reload round trip) and static priority only for outlier-degree waves
# speedup vs baseline: 1.0303x; 1.0020x over previous
_Z11agg1_kernelPKDF16_PKfS2_PKiS4_S2_S2_PDF16_PfS6_i:
	s_load_dwordx8 s[4:11], s[0:1], 0x0
	s_load_dwordx8 s[12:19], s[0:1], 0x20
	s_load_dwordx4 s[20:23], s[0:1], 0x40
	s_load_dword s24, s[0:1], 0x50
	v_lshlrev_b32_e32 v32, 2, v0
	v_readfirstlane_b32 s25, v0
	s_lshl_b32 s26, s2, 5
	v_and_b32_e32 v64, 7, v0
	v_bfe_u32 v65, v0, 3, 3
	v_and_b32_e32 v45, 31, v0
	s_lshr_b32 s25, s25, 6
	v_lshlrev_b32_e32 v1, 1, v64
	v_add_u32_e32 v46, s26, v45
	s_waitcnt lgkmcnt(0)
	global_load_dword v33, v32, s[14:15]
	global_load_dword v34, v32, s[16:17]
	s_add_i32 s28, s24, -1
	v_cmp_gt_i32_e64 s[38:39], s24, v46
	v_min_i32_e32 v46, s28, v46
	v_lshlrev_b32_e32 v47, 2, v46
	global_load_dword v44, v47, s[10:11]
	global_load_dword v48, v47, s[10:11] offset:4
	s_lshl_b32 s27, s25, 11
	v_lshlrev_b32_e32 v62, 6, v64
	v_add_u32_e32 v62, 0x2000, v62
	v_cmp_eq_u32_e64 s[34:35], 0, v64
	v_lshlrev_b32_e32 v35, 8, v64
	v_lshl_add_u32 v35, v65, 4, v35
	v_add_u32_e32 v63, s27, v35
	v_mov_b32_e32 v36, 0
	v_mov_b32_e32 v37, 0
	v_mov_b32_e32 v38, 0
	v_mov_b32_e32 v39, 0
	s_waitcnt vmcnt(2)
	ds_write2st64_b32 v32, v33, v34 offset0:32 offset1:36
	ds_write_b128 v63, v[36:39]
	ds_write_b128 v63, v[36:39] offset:128
	s_waitcnt vmcnt(0)
	v_sub_u32_e32 v48, v48, v44
	v_add_u32_e32 v48, 1, v48
	v_cndmask_b32_e64 v48, 0, v48, s[38:39]
	v_lshl_or_b32 v40, v48, 5, v45
	s_nop 1
	v_mov_b32_dpp v41, v40 quad_perm:[1,0,3,2] row_mask:0xf bank_mask:0xf
	s_mov_b32 s40, 0x99999999
	s_mov_b32 s41, 0x99999999
	v_min_u32_e32 v42, v40, v41
	v_max_u32_e32 v43, v40, v41
	v_cndmask_b32_e64 v40, v42, v43, s[40:41]
	s_nop 1
	v_mov_b32_dpp v41, v40 quad_perm:[2,3,0,1] row_mask:0xf bank_mask:0xf
	s_mov_b32 s40, 0xc3c3c3c3
	s_mov_b32 s41, 0xc3c3c3c3
	v_min_u32_e32 v42, v40, v41
	v_max_u32_e32 v43, v40, v41
	v_cndmask_b32_e64 v40, v42, v43, s[40:41]
	s_nop 1
	v_mov_b32_dpp v41, v40 quad_perm:[1,0,3,2] row_mask:0xf bank_mask:0xf
	s_mov_b32 s40, 0xa5a5a5a5
	s_mov_b32 s41, 0xa5a5a5a5
	v_min_u32_e32 v42, v40, v41
	v_max_u32_e32 v43, v40, v41
	v_cndmask_b32_e64 v40, v42, v43, s[40:41]
	ds_swizzle_b32 v41, v40 offset:swizzle(SWAP,4)
	s_waitcnt lgkmcnt(0)
	s_mov_b32 s40, 0xf00ff00f
	s_mov_b32 s41, 0xf00ff00f
	v_min_u32_e32 v42, v40, v41
	v_max_u32_e32 v43, v40, v41
	v_cndmask_b32_e64 v40, v42, v43, s[40:41]
	s_nop 1
	v_mov_b32_dpp v41, v40 quad_perm:[2,3,0,1] row_mask:0xf bank_mask:0xf
	s_mov_b32 s40, 0xcc33cc33
	s_mov_b32 s41, 0xcc33cc33
	v_min_u32_e32 v42, v40, v41
	v_max_u32_e32 v43, v40, v41
	v_cndmask_b32_e64 v40, v42, v43, s[40:41]
	s_nop 1
	v_mov_b32_dpp v41, v40 quad_perm:[1,0,3,2] row_mask:0xf bank_mask:0xf
	s_mov_b32 s40, 0xaa55aa55
	s_mov_b32 s41, 0xaa55aa55
	v_min_u32_e32 v42, v40, v41
	v_max_u32_e32 v43, v40, v41
	v_cndmask_b32_e64 v40, v42, v43, s[40:41]
	ds_swizzle_b32 v41, v40 offset:swizzle(SWAP,8)
	s_waitcnt lgkmcnt(0)
	s_mov_b32 s40, 0xff0000ff
	s_mov_b32 s41, 0xff0000ff
	v_min_u32_e32 v42, v40, v41
	v_max_u32_e32 v43, v40, v41
	v_cndmask_b32_e64 v40, v42, v43, s[40:41]
	ds_swizzle_b32 v41, v40 offset:swizzle(SWAP,4)
	s_waitcnt lgkmcnt(0)
	s_mov_b32 s40, 0xf0f00f0f
	s_mov_b32 s41, 0xf0f00f0f
	v_min_u32_e32 v42, v40, v41
	v_max_u32_e32 v43, v40, v41
	v_cndmask_b32_e64 v40, v42, v43, s[40:41]
	s_nop 1
	v_mov_b32_dpp v41, v40 quad_perm:[2,3,0,1] row_mask:0xf bank_mask:0xf
	s_mov_b32 s40, 0xcccc3333
	s_mov_b32 s41, 0xcccc3333
	v_min_u32_e32 v42, v40, v41
	v_max_u32_e32 v43, v40, v41
	v_cndmask_b32_e64 v40, v42, v43, s[40:41]
	s_nop 1
	v_mov_b32_dpp v41, v40 quad_perm:[1,0,3,2] row_mask:0xf bank_mask:0xf
	s_mov_b32 s40, 0xaaaa5555
	s_mov_b32 s41, 0xaaaa5555
	v_min_u32_e32 v42, v40, v41
	v_max_u32_e32 v43, v40, v41
	v_cndmask_b32_e64 v40, v42, v43, s[40:41]
	ds_swizzle_b32 v41, v40 offset:swizzle(SWAP,16)
	s_waitcnt lgkmcnt(0)
	s_mov_b32 s40, 0xffff
	s_mov_b32 s41, 0xffff
	v_min_u32_e32 v42, v40, v41
	v_max_u32_e32 v43, v40, v41
	v_cndmask_b32_e64 v40, v42, v43, s[40:41]
	ds_swizzle_b32 v41, v40 offset:swizzle(SWAP,8)
	s_waitcnt lgkmcnt(0)
	s_mov_b32 s40, 0xff00ff
	s_mov_b32 s41, 0xff00ff
	v_min_u32_e32 v42, v40, v41
	v_max_u32_e32 v43, v40, v41
	v_cndmask_b32_e64 v40, v42, v43, s[40:41]
	ds_swizzle_b32 v41, v40 offset:swizzle(SWAP,4)
	s_waitcnt lgkmcnt(0)
	s_mov_b32 s40, 0xf0f0f0f
	s_mov_b32 s41, 0xf0f0f0f
	v_min_u32_e32 v42, v40, v41
	v_max_u32_e32 v43, v40, v41
	v_cndmask_b32_e64 v40, v42, v43, s[40:41]
	s_nop 1
	v_mov_b32_dpp v41, v40 quad_perm:[2,3,0,1] row_mask:0xf bank_mask:0xf
	s_mov_b32 s40, 0x33333333
	s_mov_b32 s41, 0x33333333
	v_min_u32_e32 v42, v40, v41
	v_max_u32_e32 v43, v40, v41
	v_cndmask_b32_e64 v40, v42, v43, s[40:41]
	s_nop 1
	v_mov_b32_dpp v41, v40 quad_perm:[1,0,3,2] row_mask:0xf bank_mask:0xf
	s_mov_b32 s40, 0x55555555
	s_mov_b32 s41, 0x55555555
	v_min_u32_e32 v42, v40, v41
	v_max_u32_e32 v43, v40, v41
	v_cndmask_b32_e64 v40, v42, v43, s[40:41]
	s_lshl_b32 s40, s25, 3
	v_add_u32_e32 v45, s40, v65
	v_lshlrev_b32_e32 v45, 2, v45
	ds_bpermute_b32 v46, v45, v40
	s_waitcnt lgkmcnt(0)
	v_and_b32_e32 v15, 31, v46
	v_lshrrev_b32_e32 v11, 5, v46
	v_lshlrev_b32_e32 v47, 2, v15
	ds_bpermute_b32 v10, v47, v44
	v_add_u32_e32 v66, s26, v15
	v_min_i32_e32 v66, s28, v66
	v_cmp_lt_u32_e64 s[36:37], 0, v11
	v_lshlrev_b32_e32 v4, 2, v66
	v_lshlrev_b32_e32 v35, 2, v64
	v_lshl_or_b32 v35, v66, 5, v35
	global_load_dword v9, v35, s[8:9]
	v_lshrrev_b32_e32 v3, 3, v15
	v_lshlrev_b32_e32 v3, 11, v3
	v_and_b32_e32 v47, 7, v15
	v_lshl_add_u32 v3, v47, 1, v3
	v_lshl_add_u32 v3, v64, 4, v3
	v_readfirstlane_b32 s29, v11
	s_cmp_lt_i32 s29, 30
	s_cbranch_scc1 .Lagg_noprio
	s_setprio 3
.Lagg_noprio:
	s_waitcnt lgkmcnt(0)
	s_barrier
	v_add_u32_e32 v67, v10, v64
	v_lshlrev_b32_e32 v67, 2, v67
	v_mov_b32_e32 v5, s24
	v_mov_b32_e32 v6, s24
	v_mov_b32_e32 v7, s24
	v_mov_b32_e32 v8, s24
	v_mov_b32_e32 v69, s24
	v_cndmask_b32_e64 v5, v5, v66, s[34:35]
	v_cmp_gt_i32_e32 vcc, v11, v64
	s_andn2_b64 s[40:41], vcc, s[34:35]
	s_and_saveexec_b64 s[32:33], s[40:41]
	global_load_dword v5, v67, s[12:13] offset:-4
	s_mov_b64 exec, s[32:33]
	v_add_u32_e32 v68, 8, v64
	v_cmp_gt_i32_e32 vcc, v11, v68
	s_and_saveexec_b64 s[32:33], vcc
	global_load_dword v6, v67, s[12:13] offset:28
	s_mov_b64 exec, s[32:33]
	v_add_u32_e32 v68, 16, v64
	v_cmp_gt_i32_e32 vcc, v11, v68
	s_and_saveexec_b64 s[32:33], vcc
	global_load_dword v7, v67, s[12:13] offset:60
	s_mov_b64 exec, s[32:33]
	v_add_u32_e32 v68, 24, v64
	v_cmp_gt_i32_e32 vcc, v11, v68
	s_and_saveexec_b64 s[32:33], vcc
	global_load_dword v8, v67, s[12:13] offset:92
	s_mov_b64 exec, s[32:33]
	v_add_u32_e32 v68, 32, v64
	v_cmp_gt_i32_e32 vcc, v11, v68
	s_and_saveexec_b64 s[32:33], vcc
	global_load_dword v69, v67, s[12:13] offset:124
	s_mov_b64 exec, s[32:33]
	s_waitcnt vmcnt(0)
	v_lshlrev_b32_e32 v5, 4, v5
	v_lshlrev_b32_e32 v6, 4, v6
	v_lshlrev_b32_e32 v7, 4, v7
	v_lshlrev_b32_e32 v8, 4, v8
	v_lshlrev_b32_e32 v69, 4, v69
	s_mov_b32 s42, 0
	s_mov_b32 s43, 0
	s_cmp_lt_i32 s29, 3
	s_cbranch_scc1 .Lagg_first_half
	ds_swizzle_b32 v32, v5 offset:swizzle(BITMASK_PERM, "pp000")
	ds_swizzle_b32 v33, v5 offset:swizzle(BITMASK_PERM, "pp001")
	ds_swizzle_b32 v34, v5 offset:swizzle(BITMASK_PERM, "pp010")
	ds_swizzle_b32 v35, v5 offset:swizzle(BITMASK_PERM, "pp011")
	s_waitcnt lgkmcnt(0)
	v_or_b32_e32 v32, v32, v1
	v_or_b32_e32 v33, v33, v1
	v_or_b32_e32 v34, v34, v1
	v_or_b32_e32 v35, v35, v1
	global_load_ushort v36, v32, s[6:7]
	global_load_ushort v37, v33, s[6:7]
	global_load_ushort v38, v34, s[6:7]
	global_load_ushort v39, v35, s[6:7]
	v_lshlrev_b32_e32 v32, 3, v32
	v_lshlrev_b32_e32 v33, 3, v33
	v_lshlrev_b32_e32 v34, 3, v34
	v_lshlrev_b32_e32 v35, 3, v35
	global_load_dwordx4 v[40:43], v32, s[4:5]
	global_load_dwordx4 v[44:47], v33, s[4:5]
	global_load_dwordx4 v[48:51], v34, s[4:5]
	global_load_dwordx4 v[52:55], v35, s[4:5]
	s_waitcnt vmcnt(4)
	v_fma_mix_f32 v36, v36, 1.0, v9 op_sel_hi:[1,0,0]
	v_fma_mix_f32 v37, v37, 1.0, v9 op_sel_hi:[1,0,0]
	v_fma_mix_f32 v38, v38, 1.0, v9 op_sel_hi:[1,0,0]
	v_fma_mix_f32 v39, v39, 1.0, v9 op_sel_hi:[1,0,0]
	v_mul_f32_e32 v58, 0x3e4ccccd, v36
	v_mul_f32_e32 v59, 0x3e4ccccd, v37
	v_mul_f32_e32 v60, 0x3e4ccccd, v38
	v_mul_f32_e32 v61, 0x3e4ccccd, v39
	v_max_f32_e32 v36, v36, v58
	v_max_f32_e32 v37, v37, v59
	v_max_f32_e32 v38, v38, v60
	v_max_f32_e32 v39, v39, v61
	v_max3_f32 v56, v36, v37, v38
	v_max_f32_e32 v13, v56, v39
	v_sub_f32_e32 v36, v36, v13
	v_sub_f32_e32 v37, v37, v13
	v_sub_f32_e32 v38, v38, v13
	v_sub_f32_e32 v39, v39, v13
	v_exp_f32_e32 v36, v36
	v_exp_f32_e32 v37, v37
	v_exp_f32_e32 v38, v38
	v_exp_f32_e32 v39, v39
	s_nop 0
	v_add_f32_e32 v14, v36, v37
	v_add_f32_e32 v14, v14, v38
	v_add_f32_e32 v14, v14, v39
	s_waitcnt vmcnt(3)
	v_cvt_scalef32_pk_f16_fp8 v58, v40, 1.0
	v_cvt_scalef32_pk_f16_fp8 v59, v40, 1.0 op_sel:[1,0,0]
	v_cvt_scalef32_pk_f16_fp8 v60, v41, 1.0
	v_cvt_scalef32_pk_f16_fp8 v61, v41, 1.0 op_sel:[1,0,0]
	v_fma_mix_f32 v16, v58, v36, 0 op_sel_hi:[1,0,0]
	v_fma_mix_f32 v17, v58, v36, 0 op_sel:[1,0,0] op_sel_hi:[1,0,0]
	v_fma_mix_f32 v18, v59, v36, 0 op_sel_hi:[1,0,0]
	v_fma_mix_f32 v19, v59, v36, 0 op_sel:[1,0,0] op_sel_hi:[1,0,0]
	v_fma_mix_f32 v20, v60, v36, 0 op_sel_hi:[1,0,0]
	v_fma_mix_f32 v21, v60, v36, 0 op_sel:[1,0,0] op_sel_hi:[1,0,0]
	v_fma_mix_f32 v22, v61, v36, 0 op_sel_hi:[1,0,0]
	v_fma_mix_f32 v23, v61, v36, 0 op_sel:[1,0,0] op_sel_hi:[1,0,0]
	v_cvt_scalef32_pk_f16_fp8 v58, v42, 1.0
	v_cvt_scalef32_pk_f16_fp8 v59, v42, 1.0 op_sel:[1,0,0]
	v_cvt_scalef32_pk_f16_fp8 v60, v43, 1.0
	v_cvt_scalef32_pk_f16_fp8 v61, v43, 1.0 op_sel:[1,0,0]
	v_fma_mix_f32 v24, v58, v36, 0 op_sel_hi:[1,0,0]
	v_fma_mix_f32 v25, v58, v36, 0 op_sel:[1,0,0] op_sel_hi:[1,0,0]
	v_fma_mix_f32 v26, v59, v36, 0 op_sel_hi:[1,0,0]
	v_fma_mix_f32 v27, v59, v36, 0 op_sel:[1,0,0] op_sel_hi:[1,0,0]
	v_fma_mix_f32 v28, v60, v36, 0 op_sel_hi:[1,0,0]
	v_fma_mix_f32 v29, v60, v36, 0 op_sel:[1,0,0] op_sel_hi:[1,0,0]
	v_fma_mix_f32 v30, v61, v36, 0 op_sel_hi:[1,0,0]
	v_fma_mix_f32 v31, v61, v36, 0 op_sel:[1,0,0] op_sel_hi:[1,0,0]
	s_waitcnt vmcnt(2)
	v_cvt_scalef32_pk_f16_fp8 v58, v44, 1.0
	v_cvt_scalef32_pk_f16_fp8 v59, v44, 1.0 op_sel:[1,0,0]
	v_cvt_scalef32_pk_f16_fp8 v60, v45, 1.0
	v_cvt_scalef32_pk_f16_fp8 v61, v45, 1.0 op_sel:[1,0,0]
	v_fma_mix_f32 v16, v58, v37, v16 op_sel_hi:[1,0,0]
	v_fma_mix_f32 v17, v58, v37, v17 op_sel:[1,0,0] op_sel_hi:[1,0,0]
	v_fma_mix_f32 v18, v59, v37, v18 op_sel_hi:[1,0,0]
	v_fma_mix_f32 v19, v59, v37, v19 op_sel:[1,0,0] op_sel_hi:[1,0,0]
	v_fma_mix_f32 v20, v60, v37, v20 op_sel_hi:[1,0,0]
	v_fma_mix_f32 v21, v60, v37, v21 op_sel:[1,0,0] op_sel_hi:[1,0,0]
	v_fma_mix_f32 v22, v61, v37, v22 op_sel_hi:[1,0,0]
	v_fma_mix_f32 v23, v61, v37, v23 op_sel:[1,0,0] op_sel_hi:[1,0,0]
	v_cvt_scalef32_pk_f16_fp8 v58, v46, 1.0
	v_cvt_scalef32_pk_f16_fp8 v59, v46, 1.0 op_sel:[1,0,0]
	v_cvt_scalef32_pk_f16_fp8 v60, v47, 1.0
	v_cvt_scalef32_pk_f16_fp8 v61, v47, 1.0 op_sel:[1,0,0]
	v_fma_mix_f32 v24, v58, v37, v24 op_sel_hi:[1,0,0]
	v_fma_mix_f32 v25, v58, v37, v25 op_sel:[1,0,0] op_sel_hi:[1,0,0]
	v_fma_mix_f32 v26, v59, v37, v26 op_sel_hi:[1,0,0]
	v_fma_mix_f32 v27, v59, v37, v27 op_sel:[1,0,0] op_sel_hi:[1,0,0]
	v_fma_mix_f32 v28, v60, v37, v28 op_sel_hi:[1,0,0]
	v_fma_mix_f32 v29, v60, v37, v29 op_sel:[1,0,0] op_sel_hi:[1,0,0]
	v_fma_mix_f32 v30, v61, v37, v30 op_sel_hi:[1,0,0]
	v_fma_mix_f32 v31, v61, v37, v31 op_sel:[1,0,0] op_sel_hi:[1,0,0]
	s_waitcnt vmcnt(1)
	v_cvt_scalef32_pk_f16_fp8 v58, v48, 1.0
	v_cvt_scalef32_pk_f16_fp8 v59, v48, 1.0 op_sel:[1,0,0]
	v_cvt_scalef32_pk_f16_fp8 v60, v49, 1.0
	v_cvt_scalef32_pk_f16_fp8 v61, v49, 1.0 op_sel:[1,0,0]
	v_fma_mix_f32 v16, v58, v38, v16 op_sel_hi:[1,0,0]
	v_fma_mix_f32 v17, v58, v38, v17 op_sel:[1,0,0] op_sel_hi:[1,0,0]
	v_fma_mix_f32 v18, v59, v38, v18 op_sel_hi:[1,0,0]
	v_fma_mix_f32 v19, v59, v38, v19 op_sel:[1,0,0] op_sel_hi:[1,0,0]
	v_fma_mix_f32 v20, v60, v38, v20 op_sel_hi:[1,0,0]
	v_fma_mix_f32 v21, v60, v38, v21 op_sel:[1,0,0] op_sel_hi:[1,0,0]
	v_fma_mix_f32 v22, v61, v38, v22 op_sel_hi:[1,0,0]
	v_fma_mix_f32 v23, v61, v38, v23 op_sel:[1,0,0] op_sel_hi:[1,0,0]
	v_cvt_scalef32_pk_f16_fp8 v58, v50, 1.0
	v_cvt_scalef32_pk_f16_fp8 v59, v50, 1.0 op_sel:[1,0,0]
	v_cvt_scalef32_pk_f16_fp8 v60, v51, 1.0
	v_cvt_scalef32_pk_f16_fp8 v61, v51, 1.0 op_sel:[1,0,0]
	v_fma_mix_f32 v24, v58, v38, v24 op_sel_hi:[1,0,0]
	v_fma_mix_f32 v25, v58, v38, v25 op_sel:[1,0,0] op_sel_hi:[1,0,0]
	v_fma_mix_f32 v26, v59, v38, v26 op_sel_hi:[1,0,0]
	v_fma_mix_f32 v27, v59, v38, v27 op_sel:[1,0,0] op_sel_hi:[1,0,0]
	v_fma_mix_f32 v28, v60, v38, v28 op_sel_hi:[1,0,0]
	v_fma_mix_f32 v29, v60, v38, v29 op_sel:[1,0,0] op_sel_hi:[1,0,0]
	v_fma_mix_f32 v30, v61, v38, v30 op_sel_hi:[1,0,0]
	v_fma_mix_f32 v31, v61, v38, v31 op_sel:[1,0,0] op_sel_hi:[1,0,0]
	s_waitcnt vmcnt(0)
	v_cvt_scalef32_pk_f16_fp8 v58, v52, 1.0
	v_cvt_scalef32_pk_f16_fp8 v59, v52, 1.0 op_sel:[1,0,0]
	v_cvt_scalef32_pk_f16_fp8 v60, v53, 1.0
	v_cvt_scalef32_pk_f16_fp8 v61, v53, 1.0 op_sel:[1,0,0]
	v_fma_mix_f32 v16, v58, v39, v16 op_sel_hi:[1,0,0]
	v_fma_mix_f32 v17, v58, v39, v17 op_sel:[1,0,0] op_sel_hi:[1,0,0]
	v_fma_mix_f32 v18, v59, v39, v18 op_sel_hi:[1,0,0]
	v_fma_mix_f32 v19, v59, v39, v19 op_sel:[1,0,0] op_sel_hi:[1,0,0]
	v_fma_mix_f32 v20, v60, v39, v20 op_sel_hi:[1,0,0]
	v_fma_mix_f32 v21, v60, v39, v21 op_sel:[1,0,0] op_sel_hi:[1,0,0]
	v_fma_mix_f32 v22, v61, v39, v22 op_sel_hi:[1,0,0]
	v_fma_mix_f32 v23, v61, v39, v23 op_sel:[1,0,0] op_sel_hi:[1,0,0]
	v_cvt_scalef32_pk_f16_fp8 v58, v54, 1.0
	v_cvt_scalef32_pk_f16_fp8 v59, v54, 1.0 op_sel:[1,0,0]
	v_cvt_scalef32_pk_f16_fp8 v60, v55, 1.0
	v_cvt_scalef32_pk_f16_fp8 v61, v55, 1.0 op_sel:[1,0,0]
	v_fma_mix_f32 v24, v58, v39, v24 op_sel_hi:[1,0,0]
	v_fma_mix_f32 v25, v58, v39, v25 op_sel:[1,0,0] op_sel_hi:[1,0,0]
	v_fma_mix_f32 v26, v59, v39, v26 op_sel_hi:[1,0,0]
	v_fma_mix_f32 v27, v59, v39, v27 op_sel:[1,0,0] op_sel_hi:[1,0,0]
	v_fma_mix_f32 v28, v60, v39, v28 op_sel_hi:[1,0,0]
	v_fma_mix_f32 v29, v60, v39, v29 op_sel:[1,0,0] op_sel_hi:[1,0,0]
	v_fma_mix_f32 v30, v61, v39, v30 op_sel_hi:[1,0,0]
	v_fma_mix_f32 v31, v61, v39, v31 op_sel:[1,0,0] op_sel_hi:[1,0,0]
	s_sub_i32 s29, s29, 4
	s_branch .Lagg_B

.Lagg_B:
	s_cmp_lt_i32 s29, 1
	s_cbranch_scc1 .Lagg_epi
	s_cmp_lt_i32 s29, 3
	s_cbranch_scc1 .Lagg_B_half
	ds_swizzle_b32 v32, v5 offset:swizzle(BITMASK_PERM, "pp100")
	ds_swizzle_b32 v33, v5 offset:swizzle(BITMASK_PERM, "pp101")
	ds_swizzle_b32 v34, v5 offset:swizzle(BITMASK_PERM, "pp110")
	ds_swizzle_b32 v35, v5 offset:swizzle(BITMASK_PERM, "pp111")
	s_waitcnt lgkmcnt(0)
	v_or_b32_e32 v32, v32, v1
	v_or_b32_e32 v33, v33, v1
	v_or_b32_e32 v34, v34, v1
	v_or_b32_e32 v35, v35, v1
	global_load_ushort v36, v32, s[6:7]
	global_load_ushort v37, v33, s[6:7]
	global_load_ushort v38, v34, s[6:7]
	global_load_ushort v39, v35, s[6:7]
	v_lshlrev_b32_e32 v32, 3, v32
	v_lshlrev_b32_e32 v33, 3, v33
	v_lshlrev_b32_e32 v34, 3, v34
	v_lshlrev_b32_e32 v35, 3, v35
	global_load_dwordx4 v[40:43], v32, s[4:5]
	global_load_dwordx4 v[44:47], v33, s[4:5]
	global_load_dwordx4 v[48:51], v34, s[4:5]
	global_load_dwordx4 v[52:55], v35, s[4:5]
	s_waitcnt vmcnt(4)
	v_fma_mix_f32 v36, v36, 1.0, v9 op_sel_hi:[1,0,0]
	v_fma_mix_f32 v37, v37, 1.0, v9 op_sel_hi:[1,0,0]
	v_fma_mix_f32 v38, v38, 1.0, v9 op_sel_hi:[1,0,0]
	v_fma_mix_f32 v39, v39, 1.0, v9 op_sel_hi:[1,0,0]
	v_mul_f32_e32 v58, 0x3e4ccccd, v36
	v_mul_f32_e32 v59, 0x3e4ccccd, v37
	v_mul_f32_e32 v60, 0x3e4ccccd, v38
	v_mul_f32_e32 v61, 0x3e4ccccd, v39
	v_max_f32_e32 v36, v36, v58
	v_max_f32_e32 v37, v37, v59
	v_max_f32_e32 v38, v38, v60
	v_max_f32_e32 v39, v39, v61
	v_max3_f32 v56, v13, v36, v37
	v_max3_f32 v12, v56, v38, v39
	v_sub_f32_e32 v57, v13, v12
	v_sub_f32_e32 v36, v36, v12
	v_sub_f32_e32 v37, v37, v12
	v_sub_f32_e32 v38, v38, v12
	v_sub_f32_e32 v39, v39, v12
	v_exp_f32_e32 v57, v57
	v_exp_f32_e32 v36, v36
	v_exp_f32_e32 v37, v37
	v_exp_f32_e32 v38, v38
	v_exp_f32_e32 v39, v39
	v_fma_f32 v14, v14, v57, v36
	v_mul_f32_e32 v16, v16, v57
	v_mul_f32_e32 v17, v17, v57
	v_mul_f32_e32 v18, v18, v57
	v_mul_f32_e32 v19, v19, v57
	v_mul_f32_e32 v20, v20, v57
	v_mul_f32_e32 v21, v21, v57
	v_mul_f32_e32 v22, v22, v57
	v_mul_f32_e32 v23, v23, v57
	v_mul_f32_e32 v24, v24, v57
	v_mul_f32_e32 v25, v25, v57
	v_mul_f32_e32 v26, v26, v57
	v_mul_f32_e32 v27, v27, v57
	v_mul_f32_e32 v28, v28, v57
	v_mul_f32_e32 v29, v29, v57
	v_mul_f32_e32 v30, v30, v57
	v_mul_f32_e32 v31, v31, v57
	v_add_f32_e32 v14, v14, v37
	v_add_f32_e32 v14, v14, v38
	v_add_f32_e32 v14, v14, v39
	s_waitcnt vmcnt(3)
	v_cvt_scalef32_pk_f16_fp8 v58, v40, 1.0
	v_cvt_scalef32_pk_f16_fp8 v59, v40, 1.0 op_sel:[1,0,0]
	v_cvt_scalef32_pk_f16_fp8 v60, v41, 1.0
	v_cvt_scalef32_pk_f16_fp8 v61, v41, 1.0 op_sel:[1,0,0]
	v_fma_mix_f32 v16, v58, v36, v16 op_sel_hi:[1,0,0]
	v_fma_mix_f32 v17, v58, v36, v17 op_sel:[1,0,0] op_sel_hi:[1,0,0]
	v_fma_mix_f32 v18, v59, v36, v18 op_sel_hi:[1,0,0]
	v_fma_mix_f32 v19, v59, v36, v19 op_sel:[1,0,0] op_sel_hi:[1,0,0]
	v_fma_mix_f32 v20, v60, v36, v20 op_sel_hi:[1,0,0]
	v_fma_mix_f32 v21, v60, v36, v21 op_sel:[1,0,0] op_sel_hi:[1,0,0]
	v_fma_mix_f32 v22, v61, v36, v22 op_sel_hi:[1,0,0]
	v_fma_mix_f32 v23, v61, v36, v23 op_sel:[1,0,0] op_sel_hi:[1,0,0]
	v_cvt_scalef32_pk_f16_fp8 v58, v42, 1.0
	v_cvt_scalef32_pk_f16_fp8 v59, v42, 1.0 op_sel:[1,0,0]
	v_cvt_scalef32_pk_f16_fp8 v60, v43, 1.0
	v_cvt_scalef32_pk_f16_fp8 v61, v43, 1.0 op_sel:[1,0,0]
	v_fma_mix_f32 v24, v58, v36, v24 op_sel_hi:[1,0,0]
	v_fma_mix_f32 v25, v58, v36, v25 op_sel:[1,0,0] op_sel_hi:[1,0,0]
	v_fma_mix_f32 v26, v59, v36, v26 op_sel_hi:[1,0,0]
	v_fma_mix_f32 v27, v59, v36, v27 op_sel:[1,0,0] op_sel_hi:[1,0,0]
	v_fma_mix_f32 v28, v60, v36, v28 op_sel_hi:[1,0,0]
	v_fma_mix_f32 v29, v60, v36, v29 op_sel:[1,0,0] op_sel_hi:[1,0,0]
	v_fma_mix_f32 v30, v61, v36, v30 op_sel_hi:[1,0,0]
	v_fma_mix_f32 v31, v61, v36, v31 op_sel:[1,0,0] op_sel_hi:[1,0,0]
	s_waitcnt vmcnt(2)
	v_cvt_scalef32_pk_f16_fp8 v58, v44, 1.0
	v_cvt_scalef32_pk_f16_fp8 v59, v44, 1.0 op_sel:[1,0,0]
	v_cvt_scalef32_pk_f16_fp8 v60, v45, 1.0
	v_cvt_scalef32_pk_f16_fp8 v61, v45, 1.0 op_sel:[1,0,0]
	v_fma_mix_f32 v16, v58, v37, v16 op_sel_hi:[1,0,0]
	v_fma_mix_f32 v17, v58, v37, v17 op_sel:[1,0,0] op_sel_hi:[1,0,0]
	v_fma_mix_f32 v18, v59, v37, v18 op_sel_hi:[1,0,0]
	v_fma_mix_f32 v19, v59, v37, v19 op_sel:[1,0,0] op_sel_hi:[1,0,0]
	v_fma_mix_f32 v20, v60, v37, v20 op_sel_hi:[1,0,0]
	v_fma_mix_f32 v21, v60, v37, v21 op_sel:[1,0,0] op_sel_hi:[1,0,0]
	v_fma_mix_f32 v22, v61, v37, v22 op_sel_hi:[1,0,0]
	v_fma_mix_f32 v23, v61, v37, v23 op_sel:[1,0,0] op_sel_hi:[1,0,0]
	v_cvt_scalef32_pk_f16_fp8 v58, v46, 1.0
	v_cvt_scalef32_pk_f16_fp8 v59, v46, 1.0 op_sel:[1,0,0]
	v_cvt_scalef32_pk_f16_fp8 v60, v47, 1.0
	v_cvt_scalef32_pk_f16_fp8 v61, v47, 1.0 op_sel:[1,0,0]
	v_fma_mix_f32 v24, v58, v37, v24 op_sel_hi:[1,0,0]
	v_fma_mix_f32 v25, v58, v37, v25 op_sel:[1,0,0] op_sel_hi:[1,0,0]
	v_fma_mix_f32 v26, v59, v37, v26 op_sel_hi:[1,0,0]
	v_fma_mix_f32 v27, v59, v37, v27 op_sel:[1,0,0] op_sel_hi:[1,0,0]
	v_fma_mix_f32 v28, v60, v37, v28 op_sel_hi:[1,0,0]
	v_fma_mix_f32 v29, v60, v37, v29 op_sel:[1,0,0] op_sel_hi:[1,0,0]
	v_fma_mix_f32 v30, v61, v37, v30 op_sel_hi:[1,0,0]
	v_fma_mix_f32 v31, v61, v37, v31 op_sel:[1,0,0] op_sel_hi:[1,0,0]
	s_waitcnt vmcnt(1)
	v_cvt_scalef32_pk_f16_fp8 v58, v48, 1.0
	v_cvt_scalef32_pk_f16_fp8 v59, v48, 1.0 op_sel:[1,0,0]
	v_cvt_scalef32_pk_f16_fp8 v60, v49, 1.0
	v_cvt_scalef32_pk_f16_fp8 v61, v49, 1.0 op_sel:[1,0,0]
	v_fma_mix_f32 v16, v58, v38, v16 op_sel_hi:[1,0,0]
	v_fma_mix_f32 v17, v58, v38, v17 op_sel:[1,0,0] op_sel_hi:[1,0,0]
	v_fma_mix_f32 v18, v59, v38, v18 op_sel_hi:[1,0,0]
	v_fma_mix_f32 v19, v59, v38, v19 op_sel:[1,0,0] op_sel_hi:[1,0,0]
	v_fma_mix_f32 v20, v60, v38, v20 op_sel_hi:[1,0,0]
	v_fma_mix_f32 v21, v60, v38, v21 op_sel:[1,0,0] op_sel_hi:[1,0,0]
	v_fma_mix_f32 v22, v61, v38, v22 op_sel_hi:[1,0,0]
	v_fma_mix_f32 v23, v61, v38, v23 op_sel:[1,0,0] op_sel_hi:[1,0,0]
	v_cvt_scalef32_pk_f16_fp8 v58, v50, 1.0
	v_cvt_scalef32_pk_f16_fp8 v59, v50, 1.0 op_sel:[1,0,0]
	v_cvt_scalef32_pk_f16_fp8 v60, v51, 1.0
	v_cvt_scalef32_pk_f16_fp8 v61, v51, 1.0 op_sel:[1,0,0]
	v_fma_mix_f32 v24, v58, v38, v24 op_sel_hi:[1,0,0]
	v_fma_mix_f32 v25, v58, v38, v25 op_sel:[1,0,0] op_sel_hi:[1,0,0]
	v_fma_mix_f32 v26, v59, v38, v26 op_sel_hi:[1,0,0]
	v_fma_mix_f32 v27, v59, v38, v27 op_sel:[1,0,0] op_sel_hi:[1,0,0]
	v_fma_mix_f32 v28, v60, v38, v28 op_sel_hi:[1,0,0]
	v_fma_mix_f32 v29, v60, v38, v29 op_sel:[1,0,0] op_sel_hi:[1,0,0]
	v_fma_mix_f32 v30, v61, v38, v30 op_sel_hi:[1,0,0]
	v_fma_mix_f32 v31, v61, v38, v31 op_sel:[1,0,0] op_sel_hi:[1,0,0]
	s_waitcnt vmcnt(0)
	v_cvt_scalef32_pk_f16_fp8 v58, v52, 1.0
	v_cvt_scalef32_pk_f16_fp8 v59, v52, 1.0 op_sel:[1,0,0]
	v_cvt_scalef32_pk_f16_fp8 v60, v53, 1.0
	v_cvt_scalef32_pk_f16_fp8 v61, v53, 1.0 op_sel:[1,0,0]
	v_fma_mix_f32 v16, v58, v39, v16 op_sel_hi:[1,0,0]
	v_fma_mix_f32 v17, v58, v39, v17 op_sel:[1,0,0] op_sel_hi:[1,0,0]
	v_fma_mix_f32 v18, v59, v39, v18 op_sel_hi:[1,0,0]
	v_fma_mix_f32 v19, v59, v39, v19 op_sel:[1,0,0] op_sel_hi:[1,0,0]
	v_fma_mix_f32 v20, v60, v39, v20 op_sel_hi:[1,0,0]
	v_fma_mix_f32 v21, v60, v39, v21 op_sel:[1,0,0] op_sel_hi:[1,0,0]
	v_fma_mix_f32 v22, v61, v39, v22 op_sel_hi:[1,0,0]
	v_fma_mix_f32 v23, v61, v39, v23 op_sel:[1,0,0] op_sel_hi:[1,0,0]
	v_cvt_scalef32_pk_f16_fp8 v58, v54, 1.0
	v_cvt_scalef32_pk_f16_fp8 v59, v54, 1.0 op_sel:[1,0,0]
	v_cvt_scalef32_pk_f16_fp8 v60, v55, 1.0
	v_cvt_scalef32_pk_f16_fp8 v61, v55, 1.0 op_sel:[1,0,0]
	v_fma_mix_f32 v24, v58, v39, v24 op_sel_hi:[1,0,0]
	v_fma_mix_f32 v25, v58, v39, v25 op_sel:[1,0,0] op_sel_hi:[1,0,0]
	v_fma_mix_f32 v26, v59, v39, v26 op_sel_hi:[1,0,0]
	v_fma_mix_f32 v27, v59, v39, v27 op_sel:[1,0,0] op_sel_hi:[1,0,0]
	v_fma_mix_f32 v28, v60, v39, v28 op_sel_hi:[1,0,0]
	v_fma_mix_f32 v29, v60, v39, v29 op_sel:[1,0,0] op_sel_hi:[1,0,0]
	v_fma_mix_f32 v30, v61, v39, v30 op_sel_hi:[1,0,0]
	v_fma_mix_f32 v31, v61, v39, v31 op_sel:[1,0,0] op_sel_hi:[1,0,0]
	s_sub_i32 s29, s29, 4
	v_mov_b32_e32 v5, v6
	v_mov_b32_e32 v6, v7
	v_mov_b32_e32 v7, v8
	v_mov_b32_e32 v8, v69
	s_add_i32 s43, s43, 1
	s_cmp_lt_i32 s29, 1
	s_cbranch_scc1 .Lagg_epi
	s_cmp_lg_u32 s43, 5
	s_cbranch_scc1 .Lagg_A
	s_add_i32 s42, s42, 40
	s_mov_b32 s43, 0
	v_add_u32_e32 v68, s42, v64
	v_add_u32_e32 v67, v10, v68
	v_lshlrev_b32_e32 v67, 2, v67
	v_mov_b32_e32 v5, s24
	v_mov_b32_e32 v6, s24
	v_mov_b32_e32 v7, s24
	v_mov_b32_e32 v8, s24
	v_mov_b32_e32 v69, s24
	v_cmp_gt_i32_e32 vcc, v11, v68
	s_and_saveexec_b64 s[32:33], vcc
	global_load_dword v5, v67, s[12:13] offset:-4
	s_mov_b64 exec, s[32:33]
	v_add_u32_e32 v68, 8, v68
	v_cmp_gt_i32_e32 vcc, v11, v68
	s_and_saveexec_b64 s[32:33], vcc
	global_load_dword v6, v67, s[12:13] offset:28
	s_mov_b64 exec, s[32:33]
	v_add_u32_e32 v68, 8, v68
	v_cmp_gt_i32_e32 vcc, v11, v68
	s_and_saveexec_b64 s[32:33], vcc
	global_load_dword v7, v67, s[12:13] offset:60
	s_mov_b64 exec, s[32:33]
	v_add_u32_e32 v68, 8, v68
	v_cmp_gt_i32_e32 vcc, v11, v68
	s_and_saveexec_b64 s[32:33], vcc
	global_load_dword v8, v67, s[12:13] offset:92
	s_mov_b64 exec, s[32:33]
	v_add_u32_e32 v68, 8, v68
	v_cmp_gt_i32_e32 vcc, v11, v68
	s_and_saveexec_b64 s[32:33], vcc
	global_load_dword v69, v67, s[12:13] offset:124
	s_mov_b64 exec, s[32:33]
	s_waitcnt vmcnt(0)
	v_lshlrev_b32_e32 v5, 4, v5
	v_lshlrev_b32_e32 v6, 4, v6
	v_lshlrev_b32_e32 v7, 4, v7
	v_lshlrev_b32_e32 v8, 4, v8
	v_lshlrev_b32_e32 v69, 4, v69

	.amdhsa_kernel _Z11agg1_kernelPKDF16_PKfS2_PKiS4_S2_S2_PDF16_PfS6_i
		.amdhsa_group_segment_fixed_size 10240
		.amdhsa_private_segment_fixed_size 0
		.amdhsa_kernarg_size 84
		.amdhsa_user_sgpr_count 2
		.amdhsa_user_sgpr_dispatch_ptr 0
		.amdhsa_user_sgpr_queue_ptr 0
		.amdhsa_user_sgpr_kernarg_segment_ptr 1
		.amdhsa_user_sgpr_dispatch_id 0
		.amdhsa_user_sgpr_kernarg_preload_length 0
		.amdhsa_user_sgpr_kernarg_preload_offset 0
		.amdhsa_user_sgpr_private_segment_size 0
		.amdhsa_uses_dynamic_stack 0
		.amdhsa_enable_private_segment 0
		.amdhsa_system_sgpr_workgroup_id_x 1
		.amdhsa_system_sgpr_workgroup_id_y 0
		.amdhsa_system_sgpr_workgroup_id_z 0
		.amdhsa_system_sgpr_workgroup_info 0
		.amdhsa_system_vgpr_workitem_id 0
		.amdhsa_next_free_vgpr 70
		.amdhsa_next_free_sgpr 48
		.amdhsa_accum_offset 72
		.amdhsa_reserve_vcc 1
		.amdhsa_float_round_mode_32 0
		.amdhsa_float_round_mode_16_64 0
		.amdhsa_float_denorm_mode_32 3
		.amdhsa_float_denorm_mode_16_64 3
		.amdhsa_dx10_clamp 1
		.amdhsa_ieee_mode 1
		.amdhsa_fp16_overflow 0
		.amdhsa_tg_split 0
		.amdhsa_exception_fp_ieee_invalid_op 0
		.amdhsa_exception_fp_denorm_src 0
		.amdhsa_exception_fp_ieee_div_zero 0
		.amdhsa_exception_fp_ieee_overflow 0
		.amdhsa_exception_fp_ieee_underflow 0
		.amdhsa_exception_fp_ieee_inexact 0
		.amdhsa_exception_int_div_zero 0
	.end_amdhsa_kernel

amdhsa.kernels:
  - .agpr_count:     0
    .args:
      - .actual_access:  read_only
        .address_space:  global
        .offset:         0
        .size:           8
        .value_kind:     global_buffer
      - .actual_access:  read_only
        .address_space:  global
        .offset:         8
        .size:           8
        .value_kind:     global_buffer
      - .actual_access:  read_only
        .address_space:  global
        .offset:         16
        .size:           8
        .value_kind:     global_buffer
      - .actual_access:  read_only
        .address_space:  global
        .offset:         24
        .size:           8
        .value_kind:     global_buffer
      - .actual_access:  read_only
        .address_space:  global
        .offset:         32
        .size:           8
        .value_kind:     global_buffer
      - .actual_access:  read_only
        .address_space:  global
        .offset:         40
        .size:           8
        .value_kind:     global_buffer
      - .actual_access:  read_only
        .address_space:  global
        .offset:         48
        .size:           8
        .value_kind:     global_buffer
      - .actual_access:  read_only
        .address_space:  global
        .offset:         56
        .size:           8
        .value_kind:     global_buffer
      - .actual_access:  read_only
        .address_space:  global
        .offset:         64
        .size:           8
        .value_kind:     global_buffer
      - .actual_access:  read_only
        .address_space:  global
        .offset:         72
        .size:           8
        .value_kind:     global_buffer
      - .actual_access:  read_only
        .address_space:  global
        .offset:         80
        .size:           8
        .value_kind:     global_buffer
      - .actual_access:  read_only
        .address_space:  global
        .offset:         88
        .size:           8
        .value_kind:     global_buffer
      - .actual_access:  read_only
        .address_space:  global
        .offset:         96
        .size:           8
        .value_kind:     global_buffer
      - .actual_access:  write_only
        .address_space:  global
        .offset:         104
        .size:           8
        .value_kind:     global_buffer
      - .actual_access:  write_only
        .address_space:  global
        .offset:         112
        .size:           8
        .value_kind:     global_buffer
      - .actual_access:  write_only
        .address_space:  global
        .offset:         120
        .size:           8
        .value_kind:     global_buffer
      - .actual_access:  write_only
        .address_space:  global
        .offset:         128
        .size:           8
        .value_kind:     global_buffer
      - .actual_access:  write_only
        .address_space:  global
        .offset:         136
        .size:           8
        .value_kind:     global_buffer
      - .actual_access:  write_only
        .address_space:  global
        .offset:         144
        .size:           8
        .value_kind:     global_buffer
      - .actual_access:  write_only
        .address_space:  global
        .offset:         152
        .size:           8
        .value_kind:     global_buffer
      - .actual_access:  write_only
        .address_space:  global
        .offset:         160
        .size:           8
        .value_kind:     global_buffer
      - .actual_access:  write_only
        .address_space:  global
        .offset:         168
        .size:           8
        .value_kind:     global_buffer
      - .actual_access:  read_only
        .address_space:  global
        .offset:         176
        .size:           8
        .value_kind:     global_buffer
    .group_segment_fixed_size: 29696
    .kernarg_segment_align: 8
    .kernarg_segment_size: 184
    .language:       OpenCL C
    .language_version:
      - 2
      - 0
    .max_flat_workgroup_size: 512
    .name:           _Z12front_kernelPKiS0_PKfS2_S2_S2_S2_S2_S2_S2_S2_S2_S2_PjS3_PiS4_PDF16_PfS6_S4_S5_S0_
    .private_segment_fixed_size: 0
    .sgpr_count:     30
    .sgpr_spill_count: 0
    .symbol:         _Z12front_kernelPKiS0_PKfS2_S2_S2_S2_S2_S2_S2_S2_S2_S2_PjS3_PiS4_PDF16_PfS6_S4_S5_S0_.kd
    .uniform_work_group_size: 1
    .uses_dynamic_stack: false
    .vgpr_count:     80
    .vgpr_spill_count: 0
    .wavefront_size: 64
  - .agpr_count:     0
    .args:
      - .actual_access:  read_only
        .address_space:  global
        .offset:         0
        .size:           8
        .value_kind:     global_buffer
      - .actual_access:  read_only
        .address_space:  global
        .offset:         8
        .size:           8
        .value_kind:     global_buffer
      - .actual_access:  write_only
        .address_space:  global
        .offset:         16
        .size:           8
        .value_kind:     global_buffer
      - .actual_access:  write_only
        .address_space:  global
        .offset:         24
        .size:           8
        .value_kind:     global_buffer
      - .actual_access:  write_only
        .address_space:  global
        .offset:         32
        .size:           8
        .value_kind:     global_buffer
      - .actual_access:  read_only
        .address_space:  global
        .offset:         40
        .size:           8
        .value_kind:     global_buffer
      - .actual_access:  read_only
        .address_space:  global
        .offset:         48
        .size:           8
        .value_kind:     global_buffer
      - .actual_access:  write_only
        .address_space:  global
        .offset:         56
        .size:           8
        .value_kind:     global_buffer
      - .actual_access:  write_only
        .address_space:  global
        .offset:         64
        .size:           8
        .value_kind:     global_buffer
    .group_segment_fixed_size: 40960
    .kernarg_segment_align: 8
    .kernarg_segment_size: 72
    .language:       OpenCL C
    .language_version:
      - 2
      - 0
    .max_flat_workgroup_size: 512
    .name:           _Z13second_kernelPKfPKDF16_PDF16_PfS4_PKjPKiPiS9_
    .private_segment_fixed_size: 0
    .sgpr_count:     29
    .sgpr_spill_count: 0
    .symbol:         _Z13second_kernelPKfPKDF16_PDF16_PfS4_PKjPKiPiS9_.kd
    .uniform_work_group_size: 1
    .uses_dynamic_stack: false
    .vgpr_count:     64
    .vgpr_spill_count: 0
    .wavefront_size: 64
  - .agpr_count:     0
    .args:
      - .actual_access:  read_only
        .address_space:  global
        .offset:         0
        .size:           8
        .value_kind:     global_buffer
      - .actual_access:  read_only
        .address_space:  global
        .offset:         8
        .size:           8
        .value_kind:     global_buffer
      - .actual_access:  read_only
        .address_space:  global
        .offset:         16
        .size:           8
        .value_kind:     global_buffer
      - .actual_access:  read_only
        .address_space:  global
        .offset:         24
        .size:           8
        .value_kind:     global_buffer
      - .actual_access:  read_only
        .address_space:  global
        .offset:         32
        .size:           8
        .value_kind:     global_buffer
      - .actual_access:  read_only
        .address_space:  global
        .offset:         40
        .size:           8
        .value_kind:     global_buffer
      - .actual_access:  read_only
        .address_space:  global
        .offset:         48
        .size:           8
        .value_kind:     global_buffer
      - .actual_access:  write_only
        .address_space:  global
        .offset:         56
        .size:           8
        .value_kind:     global_buffer
      - .actual_access:  write_only
        .address_space:  global
        .offset:         64
        .size:           8
        .value_kind:     global_buffer
      - .actual_access:  write_only
        .address_space:  global
        .offset:         72
        .size:           8
        .value_kind:     global_buffer
      - .offset:         80
        .size:           4
        .value_kind:     by_value
    .group_segment_fixed_size: 10240
    .kernarg_segment_align: 8
    .kernarg_segment_size: 84
    .language:       OpenCL C
    .language_version:
      - 2
      - 0
    .max_flat_workgroup_size: 256
    .name:           _Z11agg1_kernelPKDF16_PKfS2_PKiS4_S2_S2_PDF16_PfS6_i
    .private_segment_fixed_size: 0
    .sgpr_count:     54
    .sgpr_spill_count: 0
    .symbol:         _Z11agg1_kernelPKDF16_PKfS2_PKiS4_S2_S2_PDF16_PfS6_i.kd
    .uniform_work_group_size: 1
    .uses_dynamic_stack: false
    .vgpr_count:     70
    .vgpr_spill_count: 0
    .wavefront_size: 64
  - .agpr_count:     0
    .args:
      - .actual_access:  read_only
        .address_space:  global
        .offset:         0
        .size:           8
        .value_kind:     global_buffer
      - .actual_access:  read_only
        .address_space:  global
        .offset:         8
        .size:           8
        .value_kind:     global_buffer
      - .actual_access:  read_only
        .address_space:  global
        .offset:         16
        .size:           8
        .value_kind:     global_buffer
      - .actual_access:  read_only
        .address_space:  global
        .offset:         24
        .size:           8
        .value_kind:     global_buffer
      - .actual_access:  read_only
        .address_space:  global
        .offset:         32
        .size:           8
        .value_kind:     global_buffer
      - .actual_access:  write_only
        .address_space:  global
        .offset:         40
        .size:           8
        .value_kind:     global_buffer
      - .offset:         48
        .size:           4
        .value_kind:     by_value
    .group_segment_fixed_size: 0
    .kernarg_segment_align: 8
    .kernarg_segment_size: 52
    .language:       OpenCL C
    .language_version:
      - 2
      - 0
    .max_flat_workgroup_size: 256
    .name:           _Z13stats2_kernelPKiS0_PKfS2_S0_P15HIP_vector_typeIfLj4EEi
    .private_segment_fixed_size: 0
    .sgpr_count:     38
    .sgpr_spill_count: 0
    .symbol:         _Z13stats2_kernelPKiS0_PKfS2_S0_P15HIP_vector_typeIfLj4EEi.kd
    .uniform_work_group_size: 1
    .uses_dynamic_stack: false
    .vgpr_count:     32
    .vgpr_spill_count: 0
    .wavefront_size: 64
  - .agpr_count:     0
    .args:
      - .actual_access:  read_only
        .address_space:  global
        .offset:         0
        .size:           8
        .value_kind:     global_buffer
      - .actual_access:  read_only
        .address_space:  global
        .offset:         8
        .size:           8
        .value_kind:     global_buffer
      - .actual_access:  read_only
        .address_space:  global
        .offset:         16
        .size:           8
        .value_kind:     global_buffer
      - .actual_access:  read_only
        .address_space:  global
        .offset:         24
        .size:           8
        .value_kind:     global_buffer
      - .actual_access:  read_only
        .address_space:  global
        .offset:         32
        .size:           8
        .value_kind:     global_buffer
      - .actual_access:  write_only
        .address_space:  global
        .offset:         40
        .size:           8
        .value_kind:     global_buffer
      - .offset:         48
        .size:           4
        .value_kind:     by_value
    .group_segment_fixed_size: 70752
    .kernarg_segment_align: 8
    .kernarg_segment_size: 52
    .language:       OpenCL C
    .language_version:
      - 2
      - 0
    .max_flat_workgroup_size: 1024
    .name:           _Z12pool2_kernelPKjPKiPKfPK15HIP_vector_typeIfLj4EEPKDF16_Pfi
    .private_segment_fixed_size: 0
    .sgpr_count:     26
    .sgpr_spill_count: 0
    .symbol:         _Z12pool2_kernelPKjPKiPKfPK15HIP_vector_typeIfLj4EEPKDF16_Pfi.kd
    .uniform_work_group_size: 1
    .uses_dynamic_stack: false
    .vgpr_count:     128
    .vgpr_spill_count: 0
    .wavefront_size: 64
  - .agpr_count:     0
    .args:
      - .actual_access:  read_only
        .address_space:  global
        .offset:         0
        .size:           8
        .value_kind:     global_buffer
      - .actual_access:  read_only
        .address_space:  global
        .offset:         8
        .size:           8
        .value_kind:     global_buffer
      - .actual_access:  read_only
        .address_space:  global
        .offset:         16
        .size:           8
        .value_kind:     global_buffer
      - .actual_access:  read_only
        .address_space:  global
        .offset:         24
        .size:           8
        .value_kind:     global_buffer
      - .actual_access:  read_only
        .address_space:  global
        .offset:         32
        .size:           8
        .value_kind:     global_buffer
      - .actual_access:  read_only
        .address_space:  global
        .offset:         40
        .size:           8
        .value_kind:     global_buffer
      - .actual_access:  read_only
        .address_space:  global
        .offset:         48
        .size:           8
        .value_kind:     global_buffer
      - .actual_access:  read_only
        .address_space:  global
        .offset:         56
        .size:           8
        .value_kind:     global_buffer
      - .actual_access:  write_only
        .address_space:  global
        .offset:         64
        .size:           8
        .value_kind:     global_buffer
    .group_segment_fixed_size: 9472
    .kernarg_segment_align: 8
    .kernarg_segment_size: 72
    .language:       OpenCL C
    .language_version:
      - 2
      - 0
    .max_flat_workgroup_size: 1024
    .name:           _Z10mlp_kernelPKfPKiS0_S0_S0_S0_S0_S0_Pf
    .private_segment_fixed_size: 0
    .sgpr_count:     76
    .sgpr_spill_count: 0
    .symbol:         _Z10mlp_kernelPKfPKiS0_S0_S0_S0_S0_S0_Pf.kd
    .uniform_work_group_size: 1
    .uses_dynamic_stack: false
    .vgpr_count:     77
    .vgpr_spill_count: 0
    .wavefront_size: 64
